# attention K/V LDS fill: all 12 global loads issued before one wait instead of 6 serialized round trips
# baseline (speedup 1.0000x reference)
; DI void phase_attn(const Frame& F, int j) {
;     ...
;             u32x4 kvr[6], vvr[6];
; #pragma unroll
;             for (int it = 0; it < 6; ++it) { const int cidx = F.tid + it * NTHR, key = cidx >> 3, part = cidx & 7, kp = q0 - 128 + key; const bool ok = kp >= 0 && kp < SEQ;
;                 const bf16_t* row = QKV + (size_t)(b * SEQ + (ok ? kp : q0)) * QKV_N + 1024 + kvh * 64 + part * 8; kvr[it] = *(const u32x4*)row; vvr[it] = *(const u32x4*)(row + 128);
;                 if (!ok) { kvr[it] = (u32x4){0u, 0u, 0u, 0u}; vvr[it] = (u32x4){0u, 0u, 0u, 0u}; } }
.LBB0_307:
	s_and_b32 s30, s17, 31
	s_lshl_b32 s10, s30, 7
	s_add_i32 s31, s10, 0xffffff80
	v_add_u32_e32 v0, s31, v116
	s_lshl_b32 s2, s17, 6
	v_cmp_gt_u32_e32 vcc, s11, v0
	v_mov_b32_e32 v26, s10
	s_and_b32 s70, s2, 0xfffff000
	v_cndmask_b32_e32 v0, v26, v0, vcc
	s_mov_b32 s4, s25
	s_bfe_u32 s25, s17, 0x10005
	v_add_u32_e32 v0, s70, v0
	v_mov_b64_e32 v[20:21], s[94:95]
	v_mad_i64_i32 v[0:1], s[6:7], v0, s3, v[20:21]
	s_lshl_b32 s28, s25, 7
	v_lshl_add_u64 v[0:1], v[0:1], 0, s[28:29]
	v_lshl_add_u64 v[4:5], v[0:1], 0, v[192:193]
	s_waitcnt vmcnt(0)
	s_barrier
	s_cmp_eq_u32 s25, s4
	s_cselect_b64 s[4:5], -1, 0
	s_or_b64 s[4:5], s[4:5], s[96:97]
	global_load_dwordx4 v[152:155], v[4:5], off offset:2048
	global_load_dwordx4 v[156:159], v[4:5], off offset:2304
	v_add_u32_e32 v204, s31, v117
	v_cmp_gt_u32_e32 vcc, s11, v204
	s_nop 1
	v_cndmask_b32_e32 v204, v26, v204, vcc
	v_add_u32_e32 v204, s70, v204
	v_mad_i64_i32 v[202:203], s[6:7], v204, s3, v[20:21]
	v_lshl_add_u64 v[202:203], v[202:203], 0, s[28:29]
	v_lshl_add_u64 v[202:203], v[202:203], 0, v[192:193]
	global_load_dwordx4 v[160:163], v[202:203], off offset:2048
	global_load_dwordx4 v[164:167], v[202:203], off offset:2304
	v_add_u32_e32 v204, s31, v118
	v_cmp_gt_u32_e32 vcc, s11, v204
	s_nop 1
	v_cndmask_b32_e32 v204, v26, v204, vcc
	v_add_u32_e32 v204, s70, v204
	v_mad_i64_i32 v[202:203], s[6:7], v204, s3, v[20:21]
	v_lshl_add_u64 v[202:203], v[202:203], 0, s[28:29]
	v_lshl_add_u64 v[202:203], v[202:203], 0, v[192:193]
	global_load_dwordx4 v[168:171], v[202:203], off offset:2048
	global_load_dwordx4 v[172:175], v[202:203], off offset:2304
	v_add_u32_e32 v204, s31, v119
	v_cmp_gt_u32_e32 vcc, s11, v204
	s_nop 1
	v_cndmask_b32_e32 v204, v26, v204, vcc
	v_add_u32_e32 v204, s70, v204
	v_mad_i64_i32 v[202:203], s[6:7], v204, s3, v[20:21]
	v_lshl_add_u64 v[202:203], v[202:203], 0, s[28:29]
	v_lshl_add_u64 v[202:203], v[202:203], 0, v[192:193]
	global_load_dwordx4 v[176:179], v[202:203], off offset:2048
	global_load_dwordx4 v[180:183], v[202:203], off offset:2304
	v_add_u32_e32 v204, s31, v120
	v_cmp_gt_u32_e32 vcc, s11, v204
	s_nop 1
	v_cndmask_b32_e32 v204, v26, v204, vcc
	v_add_u32_e32 v204, s70, v204
	v_mad_i64_i32 v[202:203], s[6:7], v204, s3, v[20:21]
	v_lshl_add_u64 v[202:203], v[202:203], 0, s[28:29]
	v_lshl_add_u64 v[202:203], v[202:203], 0, v[192:193]
	global_load_dwordx4 v[184:187], v[202:203], off offset:2048
	global_load_dwordx4 v[188:191], v[202:203], off offset:2304
	v_add_u32_e32 v204, s31, v121
	v_cmp_gt_u32_e32 vcc, s11, v204
	s_nop 1
	v_cndmask_b32_e32 v204, v26, v204, vcc
	v_add_u32_e32 v204, s70, v204
	v_mad_i64_i32 v[202:203], s[6:7], v204, s3, v[20:21]
	v_lshl_add_u64 v[202:203], v[202:203], 0, s[28:29]
	v_lshl_add_u64 v[202:203], v[202:203], 0, v[192:193]
	global_load_dwordx4 v[194:197], v[202:203], off offset:2048
	global_load_dwordx4 v[198:201], v[202:203], off offset:2304
	s_waitcnt vmcnt(0)
; #define LAS __attribute__((address_space(3)))
; DI void phase_attn(const Frame& F, int j) {
;     ...
;             for (int it = 0; it < 6; ++it) { const int cidx = F.tid + it * NTHR, key = cidx >> 3, part = cidx & 7, kp = q0 - 128 + key; const bool ok = kp >= 0 && kp < SEQ;
;                 const bf16_t* row = QKV + (size_t)(b * SEQ + (ok ? kp : q0)) * QKV_N + 1024 + kvh * 64 + part * 8; kvr[it] = *(const u32x4*)row; vvr[it] = *(const u32x4*)(row + 128);
;                 if (!ok) { kvr[it] = (u32x4){0u, 0u, 0u, 0u}; vvr[it] = (u32x4){0u, 0u, 0u, 0u}; } }
; #pragma unroll
;             for (int it = 0; it < 6; ++it) { const int cidx = F.tid + it * NTHR, key = cidx >> 3, part = cidx & 7;
;                 *(LAS u32x4*)(Ks + key * KS_STRIDE + part * 8) = kvr[it];
;                 const unsigned vw[4] = {vvr[it].x, vvr[it].y, vvr[it].z, vvr[it].w};
; #pragma unroll
;                 for (int i = 0; i < 4; ++i) { Vt[(part * 8 + 2 * i) * VT_STRIDE + key] = (bf16_t)(vw[i] & 0xffffu); Vt[(part * 8 + 2 * i + 1) * VT_STRIDE + key] = (bf16_t)(vw[i] >> 16); } }
;         }
;         if (kvh != kvh_tab) for (int i = F.tid; i < 8 * 257; i += NTHR) { const int hh = i / 257, idx = i % 257; bT[hh * 260 + idx] = F.ap->in[29][t5_bucket(idx - 128) * 16 + kvh * 8 + hh] * 1.44269504f; }
	v_add_u32_e32 v204, s31, v116
	v_cmp_gt_u32_e32 vcc, s11, v204
	s_nop 1
	v_cndmask_b32_e32 v0, 0, v152, vcc
	v_cndmask_b32_e32 v1, 0, v153, vcc
	v_cndmask_b32_e32 v2, 0, v154, vcc
	v_cndmask_b32_e32 v3, 0, v155, vcc
	v_cndmask_b32_e32 v31, 0, v156, vcc
	v_cndmask_b32_e32 v30, 0, v157, vcc
	v_cndmask_b32_e32 v29, 0, v158, vcc
	v_cndmask_b32_e32 v28, 0, v159, vcc
	v_add_u32_e32 v204, s31, v117
	v_cmp_gt_u32_e32 vcc, s11, v204
	s_nop 1
	v_cndmask_b32_e32 v4, 0, v160, vcc
	v_cndmask_b32_e32 v5, 0, v161, vcc
	v_cndmask_b32_e32 v6, 0, v162, vcc
	v_cndmask_b32_e32 v7, 0, v163, vcc
	v_cndmask_b32_e32 v35, 0, v164, vcc
	v_cndmask_b32_e32 v34, 0, v165, vcc
	v_cndmask_b32_e32 v33, 0, v166, vcc
	v_cndmask_b32_e32 v32, 0, v167, vcc
	v_add_u32_e32 v204, s31, v118
	v_cmp_gt_u32_e32 vcc, s11, v204
	s_nop 1
	v_cndmask_b32_e32 v8, 0, v168, vcc
	v_cndmask_b32_e32 v9, 0, v169, vcc
	v_cndmask_b32_e32 v10, 0, v170, vcc
	v_cndmask_b32_e32 v11, 0, v171, vcc
	v_cndmask_b32_e32 v39, 0, v172, vcc
	v_cndmask_b32_e32 v38, 0, v173, vcc
	v_cndmask_b32_e32 v37, 0, v174, vcc
	v_cndmask_b32_e32 v36, 0, v175, vcc
	v_add_u32_e32 v204, s31, v119
	v_cmp_gt_u32_e32 vcc, s11, v204
	s_nop 1
	v_cndmask_b32_e32 v12, 0, v176, vcc
	v_cndmask_b32_e32 v13, 0, v177, vcc
	v_cndmask_b32_e32 v14, 0, v178, vcc
	v_cndmask_b32_e32 v15, 0, v179, vcc
	v_cndmask_b32_e32 v43, 0, v180, vcc
	v_cndmask_b32_e32 v42, 0, v181, vcc
	v_cndmask_b32_e32 v41, 0, v182, vcc
	v_cndmask_b32_e32 v40, 0, v183, vcc
	v_add_u32_e32 v204, s31, v120
	v_cmp_gt_u32_e32 vcc, s11, v204
	s_nop 1
	v_cndmask_b32_e32 v16, 0, v184, vcc
	v_cndmask_b32_e32 v17, 0, v185, vcc
	v_cndmask_b32_e32 v18, 0, v186, vcc
	v_cndmask_b32_e32 v19, 0, v187, vcc
	v_cndmask_b32_e32 v47, 0, v188, vcc
	v_cndmask_b32_e32 v46, 0, v189, vcc
	v_cndmask_b32_e32 v45, 0, v190, vcc
	v_cndmask_b32_e32 v44, 0, v191, vcc
	v_add_u32_e32 v204, s31, v121
	v_cmp_gt_u32_e32 vcc, s11, v204
	s_nop 1
	v_cndmask_b32_e32 v20, 0, v194, vcc
	v_cndmask_b32_e32 v21, 0, v195, vcc
	v_cndmask_b32_e32 v22, 0, v196, vcc
	v_cndmask_b32_e32 v23, 0, v197, vcc
	v_cndmask_b32_e32 v24, 0, v198, vcc
	v_cndmask_b32_e32 v25, 0, v199, vcc
	v_cndmask_b32_e32 v26, 0, v200, vcc
	v_cndmask_b32_e32 v27, 0, v201, vcc
	ds_write_b128 v122, v[0:3]
	ds_write_b16 v123, v31 offset:55296
	ds_write_b16_d16_hi v123, v31 offset:56080
	ds_write_b16 v123, v30 offset:56864
	ds_write_b16_d16_hi v123, v30 offset:57648
	ds_write_b16 v123, v29 offset:58432
	ds_write_b16_d16_hi v123, v29 offset:59216
	ds_write_b16 v123, v28 offset:60000
	ds_write_b16_d16_hi v123, v28 offset:60784
	ds_write_b128 v124, v[4:7]
	ds_write_b16 v125, v35 offset:55296
	ds_write_b16_d16_hi v125, v35 offset:56080
	ds_write_b16 v125, v34 offset:56864
	ds_write_b16_d16_hi v125, v34 offset:57648
	ds_write_b16 v125, v33 offset:58432
	ds_write_b16_d16_hi v125, v33 offset:59216
	ds_write_b16 v125, v32 offset:60000
	ds_write_b16_d16_hi v125, v32 offset:60784
	ds_write_b128 v126, v[8:11]
	ds_write_b16 v127, v39 offset:55296
	ds_write_b16_d16_hi v127, v39 offset:56080
	ds_write_b16 v127, v38 offset:56864
	ds_write_b16_d16_hi v127, v38 offset:57648
	ds_write_b16 v127, v37 offset:58432
	ds_write_b16_d16_hi v127, v37 offset:59216
	ds_write_b16 v127, v36 offset:60000
	ds_write_b16_d16_hi v127, v36 offset:60784
	ds_write_b128 v128, v[12:15]
	ds_write_b16 v129, v43 offset:55296
	ds_write_b16_d16_hi v129, v43 offset:56080
	ds_write_b16 v129, v42 offset:56864
	ds_write_b16_d16_hi v129, v42 offset:57648
	ds_write_b16 v129, v41 offset:58432
	ds_write_b16_d16_hi v129, v41 offset:59216
	ds_write_b16 v129, v40 offset:60000
	ds_write_b16_d16_hi v129, v40 offset:60784
	ds_write_b128 v130, v[16:19]
	ds_write_b16 v131, v47 offset:55296
	ds_write_b16_d16_hi v131, v47 offset:56080
	ds_write_b16 v131, v46 offset:56864
	ds_write_b16_d16_hi v131, v46 offset:57648
	ds_write_b16 v131, v45 offset:58432
	ds_write_b16_d16_hi v131, v45 offset:59216
	ds_write_b16 v131, v44 offset:60000
	ds_write_b16_d16_hi v131, v44 offset:60784
	ds_write_b128 v132, v[20:23]
	ds_write_b16 v133, v24 offset:55296
	ds_write_b16_d16_hi v133, v24 offset:56080
	ds_write_b16 v133, v25 offset:56864
	ds_write_b16_d16_hi v133, v25 offset:57648
	ds_write_b16 v133, v26 offset:58432
	ds_write_b16_d16_hi v133, v26 offset:59216
	ds_write_b16 v133, v27 offset:60000
	ds_write_b16_d16_hi v133, v27 offset:60784
	s_and_saveexec_b64 s[6:7], s[4:5]
	s_xor_b64 s[4:5], exec, s[6:7]
	s_lshl_b32 s2, s25, 3
	s_or_saveexec_b64 s[74:75], s[4:5]
	v_mov_b32_e32 v0, s2
	s_xor_b64 exec, exec, s[74:75]
	s_cbranch_execz .LBB0_318
	s_load_dwordx2 s[4:5], s[92:93], 0xe8
	s_lshl_b32 s2, s25, 3
	s_mov_b64 s[8:9], -1
	v_mov_b32_e32 v0, v80
	s_mov_b64 s[6:7], exec
	v_readlane_b32 s12, v255, 20
	v_readlane_b32 s13, v255, 21
	s_and_b64 s[12:13], s[6:7], s[12:13]
	s_mov_b64 exec, s[12:13]
	s_cbranch_execz .LBB0_314
	s_mov_b32 s28, s2
	s_mov_b64 s[8:9], 0
	v_mov_b32_e32 v2, v135
	v_mov_b64_e32 v[0:1], v[80:81]
	s_movk_i32 s13, 0x80
	s_movk_i32 s71, 0x410
	s_movk_i32 s72, 0x5a
